# top-256 threshold search on full 32-bit keys: one v_cmp per key, ballots counted and summed by the scalar unit; packed-half tables and DPP reductions removed
# speedup vs baseline: 1.0122x; 1.0038x over previous
.Ltk_mk_done:
	s_mov_b32 s11, 0
	s_brev_b32 s4, 1
.Ltk_iter:
	s_or_b32 s5, s11, s4
	s_mov_b32 s7, 0
	v_cmp_ge_u32_e64 s[20:21], v2, s5
	v_cmp_ge_u32_e64 s[22:23], v3, s5
	v_cmp_ge_u32_e64 s[24:25], v4, s5
	v_cmp_ge_u32_e64 s[26:27], v5, s5
	s_bcnt1_i32_b64 s28, s[20:21]
	s_add_u32 s7, s7, s28
	s_bcnt1_i32_b64 s28, s[22:23]
	s_add_u32 s7, s7, s28
	s_bcnt1_i32_b64 s28, s[24:25]
	s_add_u32 s7, s7, s28
	s_bcnt1_i32_b64 s28, s[26:27]
	s_add_u32 s7, s7, s28
	v_cmp_ge_u32_e64 s[30:31], v6, s5
	v_cmp_ge_u32_e64 s[36:37], v7, s5
	v_cmp_ge_u32_e64 s[44:45], v8, s5
	v_cmp_ge_u32_e64 s[2:3], v9, s5
	s_bcnt1_i32_b64 s28, s[30:31]
	s_add_u32 s7, s7, s28
	s_bcnt1_i32_b64 s28, s[36:37]
	s_add_u32 s7, s7, s28
	s_bcnt1_i32_b64 s28, s[44:45]
	s_add_u32 s7, s7, s28
	s_bcnt1_i32_b64 s28, s[2:3]
	s_add_u32 s7, s7, s28
	s_cmp_lt_u32 s0, 2
	s_cbranch_scc1 .Ltk_cnt_done
	v_cmp_ge_u32_e64 s[20:21], v10, s5
	v_cmp_ge_u32_e64 s[22:23], v11, s5
	v_cmp_ge_u32_e64 s[24:25], v12, s5
	v_cmp_ge_u32_e64 s[26:27], v13, s5
	s_bcnt1_i32_b64 s28, s[20:21]
	s_add_u32 s7, s7, s28
	s_bcnt1_i32_b64 s28, s[22:23]
	s_add_u32 s7, s7, s28
	s_bcnt1_i32_b64 s28, s[24:25]
	s_add_u32 s7, s7, s28
	s_bcnt1_i32_b64 s28, s[26:27]
	s_add_u32 s7, s7, s28
	s_cmp_lt_u32 s0, 3
	s_cbranch_scc1 .Ltk_cnt_done
	v_cmp_ge_u32_e64 s[30:31], v14, s5
	v_cmp_ge_u32_e64 s[36:37], v15, s5
	v_cmp_ge_u32_e64 s[44:45], v16, s5
	v_cmp_ge_u32_e64 s[2:3], v17, s5
	s_bcnt1_i32_b64 s28, s[30:31]
	s_add_u32 s7, s7, s28
	s_bcnt1_i32_b64 s28, s[36:37]
	s_add_u32 s7, s7, s28
	s_bcnt1_i32_b64 s28, s[44:45]
	s_add_u32 s7, s7, s28
	s_bcnt1_i32_b64 s28, s[2:3]
	s_add_u32 s7, s7, s28
	s_cmp_lt_u32 s0, 4
	s_cbranch_scc1 .Ltk_cnt_done
	v_cmp_ge_u32_e64 s[20:21], v18, s5
	v_cmp_ge_u32_e64 s[22:23], v19, s5
	v_cmp_ge_u32_e64 s[24:25], v20, s5
	v_cmp_ge_u32_e64 s[26:27], v21, s5
	s_bcnt1_i32_b64 s28, s[20:21]
	s_add_u32 s7, s7, s28
	s_bcnt1_i32_b64 s28, s[22:23]
	s_add_u32 s7, s7, s28
	s_bcnt1_i32_b64 s28, s[24:25]
	s_add_u32 s7, s7, s28
	s_bcnt1_i32_b64 s28, s[26:27]
	s_add_u32 s7, s7, s28
	s_cmp_lt_u32 s0, 5
	s_cbranch_scc1 .Ltk_cnt_done
	v_cmp_ge_u32_e64 s[30:31], v22, s5
	v_cmp_ge_u32_e64 s[36:37], v23, s5
	v_cmp_ge_u32_e64 s[44:45], v24, s5
	v_cmp_ge_u32_e64 s[2:3], v25, s5
	s_bcnt1_i32_b64 s28, s[30:31]
	s_add_u32 s7, s7, s28
	s_bcnt1_i32_b64 s28, s[36:37]
	s_add_u32 s7, s7, s28
	s_bcnt1_i32_b64 s28, s[44:45]
	s_add_u32 s7, s7, s28
	s_bcnt1_i32_b64 s28, s[2:3]
	s_add_u32 s7, s7, s28
	s_cmp_lt_u32 s0, 6
	s_cbranch_scc1 .Ltk_cnt_done
	v_cmp_ge_u32_e64 s[20:21], v26, s5
	v_cmp_ge_u32_e64 s[22:23], v27, s5
	v_cmp_ge_u32_e64 s[24:25], v28, s5
	v_cmp_ge_u32_e64 s[26:27], v29, s5
	s_bcnt1_i32_b64 s28, s[20:21]
	s_add_u32 s7, s7, s28
	s_bcnt1_i32_b64 s28, s[22:23]
	s_add_u32 s7, s7, s28
	s_bcnt1_i32_b64 s28, s[24:25]
	s_add_u32 s7, s7, s28
	s_bcnt1_i32_b64 s28, s[26:27]
	s_add_u32 s7, s7, s28
	s_cmp_lt_u32 s0, 7
	s_cbranch_scc1 .Ltk_cnt_done
	v_cmp_ge_u32_e64 s[30:31], v30, s5
	v_cmp_ge_u32_e64 s[36:37], v31, s5
	v_cmp_ge_u32_e64 s[44:45], v32, s5
	v_cmp_ge_u32_e64 s[2:3], v33, s5
	s_bcnt1_i32_b64 s28, s[30:31]
	s_add_u32 s7, s7, s28
	s_bcnt1_i32_b64 s28, s[36:37]
	s_add_u32 s7, s7, s28
	s_bcnt1_i32_b64 s28, s[44:45]
	s_add_u32 s7, s7, s28
	s_bcnt1_i32_b64 s28, s[2:3]
	s_add_u32 s7, s7, s28
	s_cmp_lt_u32 s0, 8
	s_cbranch_scc1 .Ltk_cnt_done
	v_cmp_ge_u32_e64 s[20:21], v34, s5
	v_cmp_ge_u32_e64 s[22:23], v35, s5
	v_cmp_ge_u32_e64 s[24:25], v36, s5
	v_cmp_ge_u32_e64 s[26:27], v37, s5
	s_bcnt1_i32_b64 s28, s[20:21]
	s_add_u32 s7, s7, s28
	s_bcnt1_i32_b64 s28, s[22:23]
	s_add_u32 s7, s7, s28
	s_bcnt1_i32_b64 s28, s[24:25]
	s_add_u32 s7, s7, s28
	s_bcnt1_i32_b64 s28, s[26:27]
	s_add_u32 s7, s7, s28
	s_cmp_lt_u32 s0, 9
	s_cbranch_scc1 .Ltk_cnt_done
	v_cmp_ge_u32_e64 s[30:31], v38, s5
	v_cmp_ge_u32_e64 s[36:37], v39, s5
	v_cmp_ge_u32_e64 s[44:45], v40, s5
	v_cmp_ge_u32_e64 s[2:3], v41, s5
	s_bcnt1_i32_b64 s28, s[30:31]
	s_add_u32 s7, s7, s28
	s_bcnt1_i32_b64 s28, s[36:37]
	s_add_u32 s7, s7, s28
	s_bcnt1_i32_b64 s28, s[44:45]
	s_add_u32 s7, s7, s28
	s_bcnt1_i32_b64 s28, s[2:3]
	s_add_u32 s7, s7, s28
	s_cmp_lt_u32 s0, 10
	s_cbranch_scc1 .Ltk_cnt_done
	v_cmp_ge_u32_e64 s[20:21], v42, s5
	v_cmp_ge_u32_e64 s[22:23], v43, s5
	v_cmp_ge_u32_e64 s[24:25], v44, s5
	v_cmp_ge_u32_e64 s[26:27], v45, s5
	s_bcnt1_i32_b64 s28, s[20:21]
	s_add_u32 s7, s7, s28
	s_bcnt1_i32_b64 s28, s[22:23]
	s_add_u32 s7, s7, s28
	s_bcnt1_i32_b64 s28, s[24:25]
	s_add_u32 s7, s7, s28
	s_bcnt1_i32_b64 s28, s[26:27]
	s_add_u32 s7, s7, s28
	s_cmp_lt_u32 s0, 11
	s_cbranch_scc1 .Ltk_cnt_done
	v_cmp_ge_u32_e64 s[30:31], v46, s5
	v_cmp_ge_u32_e64 s[36:37], v47, s5
	v_cmp_ge_u32_e64 s[44:45], v48, s5
	v_cmp_ge_u32_e64 s[2:3], v49, s5
	s_bcnt1_i32_b64 s28, s[30:31]
	s_add_u32 s7, s7, s28
	s_bcnt1_i32_b64 s28, s[36:37]
	s_add_u32 s7, s7, s28
	s_bcnt1_i32_b64 s28, s[44:45]
	s_add_u32 s7, s7, s28
	s_bcnt1_i32_b64 s28, s[2:3]
	s_add_u32 s7, s7, s28
	s_cmp_lt_u32 s0, 12
	s_cbranch_scc1 .Ltk_cnt_done
	v_cmp_ge_u32_e64 s[20:21], v50, s5
	v_cmp_ge_u32_e64 s[22:23], v51, s5
	v_cmp_ge_u32_e64 s[24:25], v52, s5
	v_cmp_ge_u32_e64 s[26:27], v53, s5
	s_bcnt1_i32_b64 s28, s[20:21]
	s_add_u32 s7, s7, s28
	s_bcnt1_i32_b64 s28, s[22:23]
	s_add_u32 s7, s7, s28
	s_bcnt1_i32_b64 s28, s[24:25]
	s_add_u32 s7, s7, s28
	s_bcnt1_i32_b64 s28, s[26:27]
	s_add_u32 s7, s7, s28
	s_cmp_lt_u32 s0, 13
	s_cbranch_scc1 .Ltk_cnt_done
	v_cmp_ge_u32_e64 s[30:31], v54, s5
	v_cmp_ge_u32_e64 s[36:37], v55, s5
	v_cmp_ge_u32_e64 s[44:45], v56, s5
	v_cmp_ge_u32_e64 s[2:3], v57, s5
	s_bcnt1_i32_b64 s28, s[30:31]
	s_add_u32 s7, s7, s28
	s_bcnt1_i32_b64 s28, s[36:37]
	s_add_u32 s7, s7, s28
	s_bcnt1_i32_b64 s28, s[44:45]
	s_add_u32 s7, s7, s28
	s_bcnt1_i32_b64 s28, s[2:3]
	s_add_u32 s7, s7, s28
	s_cmp_lt_u32 s0, 14
	s_cbranch_scc1 .Ltk_cnt_done
	v_cmp_ge_u32_e64 s[20:21], v58, s5
	v_cmp_ge_u32_e64 s[22:23], v59, s5
	v_cmp_ge_u32_e64 s[24:25], v60, s5
	v_cmp_ge_u32_e64 s[26:27], v61, s5
	s_bcnt1_i32_b64 s28, s[20:21]
	s_add_u32 s7, s7, s28
	s_bcnt1_i32_b64 s28, s[22:23]
	s_add_u32 s7, s7, s28
	s_bcnt1_i32_b64 s28, s[24:25]
	s_add_u32 s7, s7, s28
	s_bcnt1_i32_b64 s28, s[26:27]
	s_add_u32 s7, s7, s28
	s_cmp_lt_u32 s0, 15
	s_cbranch_scc1 .Ltk_cnt_done
	v_cmp_ge_u32_e64 s[30:31], v62, s5
	v_cmp_ge_u32_e64 s[36:37], v63, s5
	v_cmp_ge_u32_e64 s[44:45], v64, s5
	v_cmp_ge_u32_e64 s[2:3], v65, s5
	s_bcnt1_i32_b64 s28, s[30:31]
	s_add_u32 s7, s7, s28
	s_bcnt1_i32_b64 s28, s[36:37]
	s_add_u32 s7, s7, s28
	s_bcnt1_i32_b64 s28, s[44:45]
	s_add_u32 s7, s7, s28
	s_bcnt1_i32_b64 s28, s[2:3]
	s_add_u32 s7, s7, s28
.Ltk_cnt_done:
	s_cmp_lt_u32 s7, 0x100
	s_cbranch_scc1 .Ltk_next
	s_mov_b32 s11, s5
	s_cmp_eq_u32 s7, 0x100
	s_cbranch_scc1 .Ltk_exact
.Ltk_next:
	s_lshr_b32 s4, s4, 1
	s_cmp_lg_u32 s4, 0
	s_cbranch_scc1 .Ltk_iter
	s_mov_b32 s10, 0
	s_add_u32 s15, s11, 1
	s_branch .Ltk_select
.Ltk_exact:
	s_mov_b32 s10, 1
	s_mov_b32 s15, s11
